# speedup vs baseline: 1.0007x; 1.0007x over previous
.LBB0_3:
	s_add_i32 s3, s2, 0xfffffe00
	s_lshr_b32 s8, s3, 3
	s_mul_i32 s9, s8, 0x2493
	s_lshr_b32 s9, s9, 16
	s_mul_i32 s10, s9, 7
	s_sub_u32 s10, s8, s10
	s_cmp_eq_u32 s10, 0
	s_cbranch_scc1 .Lcvt_work
	s_cmp_eq_u32 s10, 3
	s_cbranch_scc0 .Lcvt_notwork
	s_mov_b32 s10, 1
	s_branch .Lcvt_work
.Lcvt_notwork:
	s_cmp_lt_u32 s9, 32
	s_cbranch_scc0 .LBB0_2
	s_lshl_b32 s9, s9, 3
	s_and_b32 s11, s3, 7
	s_or_b32 s3, s9, s11
	v_cmp_eq_u32_e32 vcc, 0, v0
	v_mov_b32_e32 v1, 0
	s_cmp_eq_u32 s10, 5
	s_cbranch_scc1 .Lcvt_mb_wo
	s_cmp_eq_u32 s10, 4
	s_cbranch_scc1 .Lcvt_mb_kv
	s_cmp_eq_u32 s10, 1
	s_cbranch_scc1 .Lcvt_mb_h2
	s_cmp_eq_u32 s10, 6
	s_cbranch_scc0 .LBB0_2
	s_cmp_eq_u32 s3, 0
	s_cbranch_scc0 .LBB0_2
	s_load_dwordx2 s[6:7], s[0:1], 0x28
	v_mov_b32_e32 v2, 0
	s_waitcnt lgkmcnt(0)
	s_add_u32 s6, s6, 0xa000000
	s_addc_u32 s7, s7, 0
	s_and_saveexec_b64 s[8:9], vcc
	s_cbranch_execz .LBB0_2
	global_store_dword v1, v2, s[6:7]
	global_store_dword v1, v2, s[6:7] offset:64
	global_store_dword v1, v2, s[6:7] offset:128
	s_endpgm
